# attention loop: 70 packed f32 VALU ops beside the MFMAs split into scalar pairs (plus the earlier attention edits)
# baseline (speedup 1.0000x reference)
; #define LAS __attribute__((address_space(3)))
; __device__ __forceinline__ void phase_attn(Frame& F) {
;     ...
;         const unsigned qrow = __umul24((unsigned)(128 * cu.n + ql), (unsigned)cu.d);
;         const float c1 = 0.125f * LOG2E;
;         const float nc2 = -__builtin_amdgcn_exp2f(-(float)(cu.h + 1)) * (float)cu.d * LOG2E;
;         const bool first = cu.n == 0;
;         f32x4 St[9];
;         const f32x4 eb = (f32x4){ef[0], ef[1], ef[2], ef[3]} * nc2;
;         float mx = -INFINITY;
;         bf16x8 kf[9][2];
; #pragma unroll
;         for (int T = 0; T < 9; ++T) { LAS unsigned char* ka = kb + (16 * (w + T) + fr) * ATT_ROWB + fq * 16; kf[T][0] = *(LAS bf16x8*)ka; kf[T][1] = *(LAS bf16x8*)(ka + 64); }
;         __builtin_amdgcn_sched_barrier(0);
; #pragma unroll
;         for (int T = 0; T < 9; ++T) {
;             f32x4 sa = (f32x4){0.f, 0.f, 0.f, 0.f};
;             sa = __builtin_amdgcn_mfma_f32_16x16x32_bf16(kf[T][0], q0, sa, 0, 0, 0);
;             sa = __builtin_amdgcn_mfma_f32_16x16x32_bf16(kf[T][1], q1, sa, 0, 0, 0);
;             const float kT = (!first || w + T >= 8) ? nc2 * (float)(128 - 16 * T) : -INFINITY;
;             sa = sa * c1 + (eb + kT);
; #pragma unroll
;             for (int rg = 0; rg < 4; ++rg) {
;                 if (T == 0) sa[rg] = ef[rg] <= 0.f ? sa[rg] : -INFINITY;
;                 if (T == 8) sa[rg] = ef[rg] >= 0.f ? sa[rg] : -INFINITY;
;             }
;             St[T] = sa;
;             mx = fmaxf(mx, fmaxf(fmaxf(sa[0], sa[1]), fmaxf(sa[2], sa[3])));
;         }
.LBB0_304:
	s_mul_i32 s37, s79, 0x12000
	s_add_i32 s85, s37, 0
	s_waitcnt vmcnt(3)
	v_mov_b64_e32 v[48:49], v[4:5]
	v_mov_b64_e32 v[46:47], v[2:3]
	v_mov_b64_e32 v[44:45], v[8:9]
	v_mov_b64_e32 v[42:43], v[6:7]
	s_lshl_b32 s65, 1, s35
	s_waitcnt lgkmcnt(0)
	s_barrier
	s_add_i32 s37, s30, 1
	v_cvt_f32_u32_e32 v54, s37
	v_cvt_f32_u32_e32 v55, s65
	v_add_u32_e32 v110, s85, v82
	v_add_u32_e32 v58, v110, v90
	v_exp_f32_e64 v54, -v54
	v_add_u32_e32 v66, v110, v91
	v_add_u32_e32 v74, v110, v92
	v_add_u32_e32 v111, v110, v93
	v_mul_f32_e32 v79, v55, v54
	ds_read_b128 v[54:57], v58
	ds_read_b128 v[58:61], v58 offset:64
	ds_read_b128 v[62:65], v66
	ds_read_b128 v[66:69], v66 offset:64
	ds_read_b128 v[70:73], v74
	ds_read_b128 v[74:77], v74 offset:64
	ds_read_b128 v[112:115], v111
	ds_read_b128 v[116:119], v111 offset:64
	v_add_u32_e32 v111, v110, v94
	ds_read_b128 v[120:123], v111
	ds_read_b128 v[124:127], v111 offset:64
	v_add_u32_e32 v111, v110, v95
	ds_read_b128 v[128:131], v111
	ds_read_b128 v[132:135], v111 offset:64
	v_add_u32_e32 v111, v110, v96
	ds_read_b128 v[136:139], v111
	ds_read_b128 v[140:143], v111 offset:64
	v_add_u32_e32 v111, v110, v97
	v_add_u32_e32 v110, v110, v98
	ds_read_b128 v[144:147], v111
	ds_read_b128 v[148:151], v111 offset:64
	ds_read_b128 v[152:155], v110
	ds_read_b128 v[156:159], v110 offset:64
	s_cmp_lg_u32 s64, 0
	v_lshl_add_u32 v78, s64, 7, v86
	s_cselect_b64 s[64:65], -1, 0
	v_mul_f32_e32 v160, 0xbfb8aa3b, v79
	v_and_b32_e32 v110, 0xffffff, v78
	s_waitcnt lgkmcnt(14)
	v_mfma_f32_16x16x32_bf16 v[54:57], v[54:57], v[46:49], 0
	v_mul_f32_e32 v78, 0x43000000, v160
	s_or_b64 vcc, s[64:65], s[38:39]
	v_cndmask_b32_e32 v78, v109, v78, vcc
	v_mfma_f32_16x16x32_bf16 v[54:57], v[58:61], v[42:45], v[54:57]
	v_fma_f32 v162, v50, v160, v78
	v_fma_f32 v163, v51, v160, v78
	v_fma_f32 v79, v53, v160, v78
	v_fma_f32 v78, v52, v160, v78
	s_or_b64 vcc, s[64:65], s[40:41]
	s_nop 3
	v_fma_f32 v56, v56, s56, v78
	v_fma_f32 v57, v57, s56, v79
	v_fma_f32 v54, v54, s56, v162
	v_fma_f32 v55, v55, s56, v163
	v_cndmask_b32_e64 v164, v109, v56, s[10:11]
	v_cndmask_b32_e64 v162, v109, v54, s[6:7]
	v_cndmask_b32_e64 v163, v109, v55, s[8:9]
	v_cndmask_b32_e64 v165, v109, v57, s[12:13]
	v_mfma_f32_16x16x32_bf16 v[54:57], v[62:65], v[46:49], 0
	v_max_f32_e32 v58, v162, v163
	v_max_f32_e32 v59, v164, v165
	v_max3_f32 v62, v58, v59, s78
	v_mfma_f32_16x16x32_bf16 v[54:57], v[66:69], v[42:45], v[54:57]
	v_mul_f32_e32 v58, 0x42e00000, v160
	v_cndmask_b32_e32 v58, v109, v58, vcc
	v_fma_f32 v60, v50, v160, v58
	v_fma_f32 v61, v51, v160, v58
	v_fma_f32 v59, v53, v160, v58
	v_fma_f32 v58, v52, v160, v58
	s_or_b64 vcc, s[64:65], s[42:43]
	s_nop 2
	v_fma_f32 v166, v56, s56, v58
	v_fma_f32 v167, v57, s56, v59
	s_waitcnt lgkmcnt(13)
	v_mfma_f32_16x16x32_bf16 v[56:59], v[70:73], v[46:49], 0
	v_fma_f32 v78, v54, s56, v60
	v_fma_f32 v79, v55, s56, v61
	v_max_f32_e32 v54, v166, v167
	v_max3_f32 v63, v78, v79, v54
	s_waitcnt lgkmcnt(12)
	v_mfma_f32_16x16x32_bf16 v[54:57], v[74:77], v[42:45], v[56:59]
	s_nop 2
	v_mul_f32_e32 v58, 0x42c00000, v160
	v_cndmask_b32_e32 v58, v109, v58, vcc
	v_fma_f32 v60, v50, v160, v58
	v_fma_f32 v61, v51, v160, v58
	v_fma_f32 v59, v53, v160, v58
	v_fma_f32 v58, v52, v160, v58
	s_nop 0
	v_fma_f32 v76, v54, s56, v60
	v_fma_f32 v77, v55, s56, v61
	v_fma_f32 v74, v56, s56, v58
	v_fma_f32 v75, v57, s56, v59
	s_waitcnt lgkmcnt(11)
	v_mfma_f32_16x16x32_bf16 v[54:57], v[112:115], v[46:49], 0
	v_max_f32_e32 v58, v74, v75
	v_max3_f32 v58, v76, v77, v58
	v_max3_f32 v62, v62, v63, v58
	s_waitcnt lgkmcnt(10)
	v_mfma_f32_16x16x32_bf16 v[54:57], v[116:119], v[42:45], v[54:57]
	v_mul_f32_e32 v58, 0x42a00000, v160
	s_or_b64 vcc, s[64:65], s[44:45]
	v_cndmask_b32_e32 v58, v109, v58, vcc
	v_fma_f32 v60, v50, v160, v58
	v_fma_f32 v61, v51, v160, v58
	v_fma_f32 v59, v53, v160, v58
	v_fma_f32 v58, v52, v160, v58
	s_nop 2
	v_fma_f32 v72, v54, s56, v60
	v_fma_f32 v73, v55, s56, v61
	v_fma_f32 v70, v56, s56, v58
	v_fma_f32 v71, v57, s56, v59
	s_waitcnt lgkmcnt(9)
	v_mfma_f32_16x16x32_bf16 v[56:59], v[120:123], v[46:49], 0
	v_max_f32_e32 v54, v70, v71
	v_max3_f32 v63, v72, v73, v54
	s_or_b64 vcc, s[64:65], s[46:47]
	s_waitcnt lgkmcnt(8)
	v_mfma_f32_16x16x32_bf16 v[54:57], v[124:127], v[42:45], v[56:59]
	s_nop 2
	v_mul_f32_e32 v58, 0x42800000, v160
	v_cndmask_b32_e32 v58, v109, v58, vcc
	v_fma_f32 v60, v50, v160, v58
	v_fma_f32 v61, v51, v160, v58
	v_fma_f32 v59, v53, v160, v58
	v_fma_f32 v58, v52, v160, v58
	s_nop 0
	v_fma_f32 v68, v54, s56, v60
	v_fma_f32 v69, v55, s56, v61
	v_fma_f32 v66, v56, s56, v58
	v_fma_f32 v67, v57, s56, v59
	s_waitcnt lgkmcnt(7)
	v_mfma_f32_16x16x32_bf16 v[54:57], v[128:131], v[46:49], 0
	v_max_f32_e32 v58, v66, v67
	v_max3_f32 v58, v68, v69, v58
	v_max3_f32 v111, v62, v63, v58
	s_waitcnt lgkmcnt(6)
	v_mfma_f32_16x16x32_bf16 v[54:57], v[132:135], v[42:45], v[54:57]
	v_mul_f32_e32 v58, 0x42400000, v160
	s_or_b64 vcc, s[64:65], s[48:49]
	v_cndmask_b32_e32 v58, v109, v58, vcc
	v_fma_f32 v60, v50, v160, v58
	v_fma_f32 v61, v51, v160, v58
	v_fma_f32 v59, v53, v160, v58
	v_fma_f32 v58, v52, v160, v58
	s_nop 2
	v_fma_f32 v64, v54, s56, v60
	v_fma_f32 v65, v55, s56, v61
	v_fma_f32 v62, v56, s56, v58
	v_fma_f32 v63, v57, s56, v59
	s_waitcnt lgkmcnt(5)
	v_mfma_f32_16x16x32_bf16 v[56:59], v[136:139], v[46:49], 0
	v_max_f32_e32 v54, v62, v63
	v_max3_f32 v112, v64, v65, v54
	s_or_b64 vcc, s[64:65], s[50:51]
	s_waitcnt lgkmcnt(4)
	v_mfma_f32_16x16x32_bf16 v[54:57], v[140:143], v[42:45], v[56:59]
	s_nop 2
	v_mul_f32_e32 v58, 0x42000000, v160
	v_cndmask_b32_e32 v58, v109, v58, vcc
	v_fma_f32 v60, v50, v160, v58
	v_fma_f32 v61, v51, v160, v58
	v_fma_f32 v59, v53, v160, v58
	v_fma_f32 v58, v52, v160, v58
	s_nop 0
	v_fma_f32 v60, v54, s56, v60
	v_fma_f32 v61, v55, s56, v61
	v_fma_f32 v58, v56, s56, v58
	v_fma_f32 v59, v57, s56, v59
	s_waitcnt lgkmcnt(3)
; __device__ __forceinline__ void phase_attn(Frame& F) {
;     ...
;             LAS unsigned char* ob = F.lds + (buf ^ 1) * ABUF;
; #pragma unroll
;             for (int jj = 0; jj < 4; ++jj) { const int ch = tid + 512 * jj, row = ch >> 3, c16 = ch & 7;
;                 *(LAS u32x4*)(ob + row * ATT_ROWB + c16 * 16) = kr[jj]; *(LAS u32x4*)(ob + ATT_VOFF + row * ATT_ROWB + c16 * 16) = vr[jj]; }
;         }
;         const AttnUnit nu = un;
;         un = attn_decode(x8 * PER_X + (jl + 2 * G8 < jlast ? jl + 2 * G8 : jlast)); attn_issue(qkv, un, tid, kr, vr);
;         { const char* qb = (const char*)qkv + (((size_t)nu.b * SEQ + nu.r) * NPROJ + nu.h * 64) * 2; const unsigned qo = __umul24((unsigned)(128 * nu.n + ql), (unsigned)nu.d * (NPROJ * 2)) + 16u * fq;
;           qn0 = *(const bf16x8*)(qb + qo); qn1 = *(const bf16x8*)(qb + qo + 64); }
;         const unsigned qrow = __umul24((unsigned)(128 * cu.n + ql), (unsigned)cu.d);
;         const float c1 = 0.125f * LOG2E;
;         const float nc2 = -__builtin_amdgcn_exp2f(-(float)(cu.h + 1)) * (float)cu.d * LOG2E;
;         const bool first = cu.n == 0;
;         f32x4 St[9];
;         const f32x4 eb = (f32x4){ef[0], ef[1], ef[2], ef[3]} * nc2;
;         float mx = -INFINITY;
;         bf16x8 kf[9][2];
; #pragma unroll
;         for (int T = 0; T < 9; ++T) { LAS unsigned char* ka = kb + (16 * (w + T) + fr) * ATT_ROWB + fq * 16; kf[T][0] = *(LAS bf16x8*)ka; kf[T][1] = *(LAS bf16x8*)(ka + 64); }
;         __builtin_amdgcn_sched_barrier(0);
; #pragma unroll
;         for (int T = 0; T < 9; ++T) {
;             f32x4 sa = (f32x4){0.f, 0.f, 0.f, 0.f};
;             sa = __builtin_amdgcn_mfma_f32_16x16x32_bf16(kf[T][0], q0, sa, 0, 0, 0);
;             sa = __builtin_amdgcn_mfma_f32_16x16x32_bf16(kf[T][1], q1, sa, 0, 0, 0);
;             const float kT = (!first || w + T >= 8) ? nc2 * (float)(128 - 16 * T) : -INFINITY;
;             sa = sa * c1 + (eb + kT);
; #pragma unroll
;             for (int rg = 0; rg < 4; ++rg) {
;                 if (T == 0) sa[rg] = ef[rg] <= 0.f ? sa[rg] : -INFINITY;
;                 if (T == 8) sa[rg] = ef[rg] >= 0.f ? sa[rg] : -INFINITY;
;             }
;             St[T] = sa;
;             mx = fmaxf(mx, fmaxf(fmaxf(sa[0], sa[1]), fmaxf(sa[2], sa[3])));
;         }
;         mx = fmaxf(mx, __shfl_xor(mx, 16)); mx = fmaxf(mx, __shfl_xor(mx, 32));
;         f32x4 lv = (f32x4){0.f, 0.f, 0.f, 0.f};
	v_mfma_f32_16x16x32_bf16 v[54:57], v[144:147], v[46:49], 0
	v_max_f32_e32 v113, v58, v59
	v_max3_f32 v113, v60, v61, v113
	v_max3_f32 v111, v111, v112, v113
	s_waitcnt lgkmcnt(1)
	v_mfma_f32_16x16x32_bf16 v[46:49], v[152:155], v[46:49], 0
	s_or_b64 vcc, s[64:65], s[52:53]
	v_add_u32_e32 v144, s85, v89
	v_add_u32_e32 v130, v144, v99
	v_mfma_f32_16x16x32_bf16 v[112:115], v[148:151], v[42:45], v[54:57]
	v_add_u32_e32 v140, v144, v100
	v_add_u32_e32 v145, v144, v101
	s_nop 0
	v_mul_f32_e32 v54, 0x41800000, v160
	s_waitcnt lgkmcnt(0)
	v_mfma_f32_16x16x32_bf16 v[42:45], v[156:159], v[42:45], v[46:49]
	s_add_i32 s37, s77, s70
	s_xor_b32 s79, s79, 1
	s_min_i32 s37, s37, s71
	s_mul_i32 s58, s79, 0x12000
	s_add_i32 s37, s37, s3
	v_add_u32_e32 v2, s58, v84
	s_mul_hi_i32 s58, s37, 0x2aaaaaab
	s_lshr_b32 s59, s58, 31
	s_ashr_i32 s58, s58, 4
	s_add_i32 s59, s58, s59
	s_mul_i32 s58, s59, 0x60
	s_sub_i32 s37, s37, s58
	s_ashr_i32 s58, s59, 3
	s_and_b32 s80, s59, 7
	v_add_u32_e32 v3, v2, v83
	s_cmp_gt_i32 s37, 31
	ds_write_b128 v3, v[38:41]
	ds_write_b128 v3, v[34:37] offset:36864
	v_add_u32_e32 v3, v2, v85
	s_cselect_b64 s[82:83], -1, 0
	s_cmp_gt_i32 s37, 63
	ds_write_b128 v3, v[30:33]
	ds_write_b128 v3, v[26:29] offset:36864
	v_add_u32_e32 v3, v2, v87
	v_add_u32_e32 v2, v2, v88
	s_cselect_b64 s[86:87], -1, 0
	ds_write_b128 v3, v[22:25]
	ds_write_b128 v3, v[18:21] offset:36864
	ds_write_b128 v2, v[14:17]
	ds_write_b128 v2, v[10:13] offset:36864
	v_cndmask_b32_e64 v2, 0, 1, s[86:87]
	s_cmp_lg_u64 s[82:83], 0
	v_readfirstlane_b32 s59, v2
	s_addc_u32 s81, s59, 0
	s_lshl_b32 s59, s81, 5
	s_lshl_b32 s82, s81, 1
	s_sub_i32 s37, s37, s59
	s_sub_i32 s59, 5, s82
	s_ashr_i32 s83, s37, s59
	s_lshl_b32 s59, -1, s59
	s_andn2_b32 s84, s37, s59
	s_ashr_i32 s59, s58, 31
	s_lshl_b64 s[86:87], s[58:59], 12
	s_ashr_i32 s37, s83, 31
	s_add_u32 s59, s86, s83
	s_addc_u32 s37, s87, s37
	s_mulk_i32 s37, 0xa00
	s_mul_hi_u32 s86, s59, 0xa00
	s_add_i32 s87, s86, s37
	s_mulk_i32 s59, 0xa00
	s_lshl_b32 s37, s80, 6
	s_or_b32 s86, s59, s37
	s_lshl_b64 s[86:87], s[86:87], 1
	s_add_u32 s37, s33, s86
	s_addc_u32 s59, s66, s87
	s_add_u32 s86, s37, 0x400
	s_addc_u32 s87, s59, 0
	s_lshl_b32 s59, s84, 7
	v_add_u32_e32 v2, s59, v81
	s_lshl_b32 s37, 0x1400, s82
	v_max_i32_e32 v3, 0, v2
	v_mul_u32_u24_e32 v3, s37, v3
	v_or_b32_e32 v3, v3, v80
	global_load_dwordx4 v[38:41], v3, s[86:87]
	global_load_dwordx4 v[34:37], v3, s[86:87] offset:1024
	v_max_i32_e32 v3, 0xffffffc0, v2
	v_add_u32_e32 v3, 64, v3
	v_mul_u32_u24_e32 v3, s37, v3
	v_or_b32_e32 v3, v3, v80
	global_load_dwordx4 v[30:33], v3, s[86:87]
	global_load_dwordx4 v[26:29], v3, s[86:87] offset:1024
	v_add_u32_e32 v3, s59, v1
	v_max_i32_e32 v2, 0xffffff40, v2
	v_max_i32_e32 v3, 0, v3
	v_add_u32_e32 v2, 0xc0, v2
	v_mul_u32_u24_e32 v3, s37, v3
	v_mul_u32_u24_e32 v2, s37, v2
	v_or_b32_e32 v3, v3, v80
	v_or_b32_e32 v2, v2, v80
	s_ashr_i32 s37, s36, 31
	global_load_dwordx4 v[22:25], v3, s[86:87]
	global_load_dwordx4 v[18:21], v3, s[86:87] offset:1024
	global_load_dwordx4 v[14:17], v2, s[86:87]
	global_load_dwordx4 v[10:13], v2, s[86:87] offset:1024
	s_lshl_b64 s[86:87], s[36:37], 12
	s_ashr_i32 s37, s73, 31
	s_add_u32 s59, s86, s73
	s_addc_u32 s37, s87, s37
	s_mulk_i32 s37, 0xa00
	s_mul_hi_u32 s86, s59, 0xa00
	s_add_i32 s87, s86, s37
	s_mulk_i32 s59, 0xa00
	s_lshl_b32 s37, s75, 6
	s_or_b32 s86, s59, s37
	s_lshl_b64 s[86:87], s[86:87], 1
	s_add_u32 s86, s33, s86
	s_addc_u32 s87, s66, s87
	s_lshl_b32 s37, 0x1400, s74
	v_lshl_add_u32 v2, s76, 7, v86
	s_and_b32 s37, s37, 0x555400
	v_mul_u32_u24_e32 v2, s37, v2
	v_or_b32_e32 v6, v2, v82
	global_load_dwordx4 v[2:5], v6, s[86:87]
	s_nop 0
	global_load_dwordx4 v[6:9], v6, s[86:87] offset:64
	v_cndmask_b32_e32 v54, v109, v54, vcc
	s_or_b64 vcc, s[64:65], s[54:55]
	v_fma_f32 v56, v50, v160, v54
	v_fma_f32 v57, v51, v160, v54
	v_mul_f32_e32 v46, 0, v160
	v_cndmask_b32_e32 v46, v109, v46, vcc
	v_fma_f32 v48, v50, v160, v46
	v_fma_f32 v49, v51, v160, v46
	v_fma_f32 v47, v53, v160, v46
	v_fma_f32 v46, v52, v160, v46
	v_fma_f32 v55, v53, v160, v54
	v_fma_f32 v54, v52, v160, v54
	v_fma_f32 v44, v44, s56, v46
	v_fma_f32 v45, v45, s56, v47
	v_fma_f32 v42, v42, s56, v48
	v_fma_f32 v43, v43, s56, v49
	v_cndmask_b32_e64 v48, v109, v44, s[18:19]
	v_and_b32_e32 v44, 64, v108
	v_fma_f32 v54, v114, s56, v54
	v_fma_f32 v55, v115, s56, v55
	v_cndmask_b32_e64 v47, v109, v43, s[16:17]
	v_cndmask_b32_e64 v49, v109, v45, s[20:21]
	v_xor_b32_e32 v43, 16, v108
	v_add_u32_e32 v44, 64, v44
	v_fma_f32 v56, v112, s56, v56
	v_fma_f32 v57, v113, s56, v57
	v_max_f32_e32 v112, v54, v55
	v_cndmask_b32_e64 v46, v109, v42, s[14:15]
	v_max_f32_e32 v42, v48, v49
	v_cmp_lt_i32_e32 vcc, v43, v44
	v_max3_f32 v112, v56, v57, v112
	v_max3_f32 v42, v46, v47, v42
	v_cndmask_b32_e32 v43, v108, v43, vcc
	v_max3_f32 v42, v111, v112, v42
	v_lshlrev_b32_e32 v142, 2, v43
	v_mov_b32_e32 v168, v42
	s_nop 1
	v_permlane16_swap_b32_e32 v168, v42
	v_max_f32_e32 v42, v42, v168
	v_xor_b32_e32 v43, 32, v108
	v_cmp_lt_i32_e32 vcc, v43, v44
	s_nop 1
	v_cndmask_b32_e32 v43, v108, v43, vcc
	v_lshlrev_b32_e32 v143, 2, v43
	v_mov_b32_e32 v168, v42
	s_nop 1
	v_permlane32_swap_b32_e32 v168, v42
	v_max_f32_e32 v111, v42, v168
	v_xor_b32_e32 v42, 0x80000000, v111
	v_mov_b32_e32 v43, v42
	v_mov_b32_e32 v44, v42
	v_mov_b32_e32 v45, v42
	ds_read_b64_tr_b16 v[120:121], v130 offset:36864
	v_add_f32_e32 v118, v166, v44
	v_add_f32_e32 v119, v167, v45
	v_add_f32_e32 v112, v164, v44
	v_add_f32_e32 v113, v165, v45
	v_exp_f32_e32 v126, v118
	v_exp_f32_e32 v127, v119
	ds_read_b64_tr_b16 v[118:119], v130 offset:36872
	v_add_f32_e32 v114, v162, v42
	v_add_f32_e32 v115, v163, v43
	v_exp_f32_e32 v112, v112
	v_exp_f32_e32 v114, v114
	v_exp_f32_e32 v113, v113
	v_exp_f32_e32 v115, v115
	ds_read_b64_tr_b16 v[128:129], v130 offset:36928
	ds_read_b64_tr_b16 v[130:131], v130 offset:36936
	v_add_f32_e32 v134, v76, v42
	v_add_f32_e32 v135, v77, v43
	v_cvt_pk_bf16_f32 v123, v112, v113
	v_cvt_pk_bf16_f32 v122, v114, v115
	v_add_f32_e32 v116, 0, v112
	v_add_f32_e32 v117, 0, v113
	v_add_f32_e32 v124, 0, v114
	v_add_f32_e32 v125, 0, v115
	s_waitcnt lgkmcnt(3)
; #define LAS __attribute__((address_space(3)))
; __device__ __forceinline__ unsigned cvt_pk_bf16(float lo, float hi) { const f32x2_t v = {lo, hi}; return __builtin_bit_cast(unsigned, __builtin_convertvector(v, bf16x2_t)); }
; __device__ __forceinline__ float fast_exp2(float x) { return __builtin_amdgcn_exp2f(x); }
; __device__ __forceinline__ s16x4 tr_read(LAS unsigned char* p) { return __builtin_bit_cast(s16x4, __builtin_amdgcn_ds_read_tr16_b64_v4i16((LAS s16x4*)p)); }
; __device__ __forceinline__ void phase_attn(Frame& F) {
;     ...
;         for (int T = 0; T < 9; ++T) { const f32x4 d = St[T] + nmx; f32x4 pv; pv.x = fast_exp2(d.x); pv.y = fast_exp2(d.y); pv.z = fast_exp2(d.z); pv.w = fast_exp2(d.w); St[T] = pv; lv = lv + pv; }
;         float l = (lv.x + lv.y) + (lv.z + lv.w);
;         l += __shfl_xor(l, 16); l += __shfl_xor(l, 32);
;         f32x4 O[4];
; #pragma unroll
;         for (int dt = 0; dt < 4; ++dt) O[dt] = (f32x4){0.f, 0.f, 0.f, 0.f};
; #pragma unroll
;         for (int T = 0; T < 9; ++T) {
;             u32x2 pw; pw.x = cvt_pk_bf16(St[T][0], St[T][1]); pw.y = cvt_pk_bf16(St[T][2], St[T][3]);
;             const s16x4 pb = __builtin_bit_cast(s16x4, pw);
;             LAS unsigned char* va = kb + ATT_VOFF + (16 * (w + T) + 4 * fq + (fr >> 2)) * ATT_ROWB + (8 * (fr & 3)) * 2;
; #pragma unroll
;             for (int dt = 0; dt < 4; ++dt) O[dt] = __builtin_amdgcn_mfma_f32_16x16x16bf16_1k(tr_read(va + 64 * (dt >> 1) + 8 * (dt & 1)), pb, O[dt], 0, 0, 0);
;         }
	v_mfma_f32_16x16x16_bf16 v[112:115], v[120:121], v[122:123], 0
	v_add_f32_e64 v120, v74, v44
	v_add_f32_e64 v121, v75, v45
	v_add_f32_e32 v132, v126, v116
	v_add_f32_e32 v133, v127, v117
	v_exp_f32_e32 v136, v120
	s_waitcnt lgkmcnt(2)
	v_mfma_f32_16x16x16_bf16 v[116:119], v[118:119], v[122:123], 0
	v_exp_f32_e32 v137, v121
	v_add_f32_e32 v78, v78, v42
	v_add_f32_e32 v79, v79, v43
	v_cvt_pk_bf16_f32 v139, v126, v127
	s_waitcnt lgkmcnt(1)
	v_mfma_f32_16x16x16_bf16 v[74:77], v[128:129], v[122:123], 0
	ds_read_b64_tr_b16 v[128:129], v140 offset:36864
	v_exp_f32_e32 v78, v78
	v_exp_f32_e32 v79, v79
	s_waitcnt lgkmcnt(1)
	v_mfma_f32_16x16x16_bf16 v[120:123], v[130:131], v[122:123], 0
	ds_read_b64_tr_b16 v[130:131], v140 offset:36872
	ds_read_b64_tr_b16 v[126:127], v140 offset:36928
	ds_read_b64_tr_b16 v[140:141], v140 offset:36936
	v_cvt_pk_bf16_f32 v138, v78, v79
	v_exp_f32_e32 v134, v134
	v_exp_f32_e32 v135, v135
	s_waitcnt lgkmcnt(3)
	v_mfma_f32_16x16x16_bf16 v[112:115], v[128:129], v[138:139], v[112:115]
	v_add_f32_e64 v128, v70, v44
	v_add_f32_e64 v129, v71, v45
	v_add_f32_e32 v78, v78, v124
	v_add_f32_e32 v79, v79, v125
	v_add_f32_e32 v124, v136, v132
	v_add_f32_e32 v125, v137, v133
	s_waitcnt lgkmcnt(2)
	v_mfma_f32_16x16x16_bf16 v[116:119], v[130:131], v[138:139], v[116:119]
	v_add_f32_e64 v130, v72, v42
	v_add_f32_e64 v131, v73, v43
	v_add_f32_e32 v78, v134, v78
	v_add_f32_e32 v79, v135, v79
	v_exp_f32_e32 v128, v128
	s_waitcnt lgkmcnt(1)
	v_mfma_f32_16x16x16_bf16 v[70:73], v[126:127], v[138:139], v[74:77]
	ds_read_b64_tr_b16 v[126:127], v145 offset:36864
	v_exp_f32_e32 v129, v129
	v_add_f32_e32 v48, v44, v48
	v_add_f32_e32 v49, v45, v49
	s_waitcnt lgkmcnt(1)
	v_mfma_f32_16x16x16_bf16 v[74:77], v[140:141], v[138:139], v[120:123]
	v_add_f32_e64 v124, v128, v124
	v_add_f32_e64 v125, v129, v125
	s_nop 0
	ds_read_b64_tr_b16 v[120:121], v145 offset:36872
	v_cvt_pk_bf16_f32 v122, v134, v135
	ds_read_b64_tr_b16 v[132:133], v145 offset:36928
	ds_read_b64_tr_b16 v[134:135], v145 offset:36936
	v_cvt_pk_bf16_f32 v123, v136, v137
	v_add_u32_e32 v136, v144, v102
	s_waitcnt lgkmcnt(3)
	v_mfma_f32_16x16x16_bf16 v[112:115], v[126:127], v[122:123], v[112:115]
	v_exp_f32_e32 v126, v130
	v_exp_f32_e32 v127, v131
	v_add_f32_e32 v130, v68, v42
	v_add_f32_e32 v131, v69, v43
	s_waitcnt lgkmcnt(2)
	v_mfma_f32_16x16x16_bf16 v[116:119], v[120:121], v[122:123], v[116:119]
	v_add_f32_e64 v120, v66, v44
	v_add_f32_e64 v121, v67, v45
	v_add_f32_e32 v78, v126, v78
	v_add_f32_e32 v79, v127, v79
	v_exp_f32_e32 v130, v130
	s_waitcnt lgkmcnt(1)
	v_mfma_f32_16x16x16_bf16 v[66:69], v[132:133], v[122:123], v[70:73]
	ds_read_b64_tr_b16 v[132:133], v136 offset:36864
	v_exp_f32_e32 v120, v120
	v_exp_f32_e32 v121, v121
	s_waitcnt lgkmcnt(1)
	v_mfma_f32_16x16x16_bf16 v[70:73], v[134:135], v[122:123], v[74:77]
	ds_read_b64_tr_b16 v[122:123], v136 offset:36872
	v_cvt_pk_bf16_f32 v134, v126, v127
	v_cvt_pk_bf16_f32 v135, v128, v129
	ds_read_b64_tr_b16 v[128:129], v136 offset:36928
	ds_read_b64_tr_b16 v[136:137], v136 offset:36936
	s_waitcnt lgkmcnt(3)
	v_mfma_f32_16x16x16_bf16 v[74:77], v[132:133], v[134:135], v[112:115]
	v_add_u32_e32 v132, v144, v103
	ds_read_b64_tr_b16 v[126:127], v132 offset:36872
	v_exp_f32_e32 v131, v131
	s_waitcnt lgkmcnt(3)
	v_mfma_f32_16x16x16_bf16 v[112:115], v[122:123], v[134:135], v[116:119]
	ds_read_b64_tr_b16 v[122:123], v132 offset:36864
	v_add_f32_e32 v124, v120, v124
	v_add_f32_e32 v125, v121, v125
	v_add_f32_e32 v78, v130, v78
	v_add_f32_e32 v79, v131, v79
	v_add_f32_e32 v116, v62, v44
	v_add_f32_e32 v117, v63, v45
	v_add_f32_e32 v118, v64, v42
	v_add_f32_e32 v119, v65, v43
	s_waitcnt lgkmcnt(3)
	v_mfma_f32_16x16x16_bf16 v[62:65], v[128:129], v[134:135], v[66:69]
	v_exp_f32_e32 v116, v116
	v_exp_f32_e32 v117, v117
	v_cvt_pk_bf16_f32 v128, v130, v131
	v_cvt_pk_bf16_f32 v129, v120, v121
	ds_read_b64_tr_b16 v[120:121], v132 offset:36928
	ds_read_b64_tr_b16 v[130:131], v132 offset:36936
	v_add_u32_e32 v132, v144, v104
	s_waitcnt lgkmcnt(4)
	v_mfma_f32_16x16x16_bf16 v[66:69], v[136:137], v[134:135], v[70:73]
	v_exp_f32_e32 v118, v118
	v_exp_f32_e32 v119, v119
	s_waitcnt lgkmcnt(2)
	v_mfma_f32_16x16x16_bf16 v[70:73], v[122:123], v[128:129], v[74:77]
	v_add_f32_e64 v122, v116, v124
	v_add_f32_e64 v123, v117, v125
	ds_read_b64_tr_b16 v[124:125], v132 offset:36872
	v_add_f32_e32 v78, v118, v78
	v_add_f32_e32 v79, v119, v79
	v_mfma_f32_16x16x16_bf16 v[74:77], v[126:127], v[128:129], v[112:115]
	v_cvt_pk_bf16_f32 v127, v116, v117
	v_cvt_pk_bf16_f32 v126, v118, v119
	s_nop 0
	v_add_f32_e32 v112, v58, v44
	v_add_f32_e32 v113, v59, v45
	v_add_f32_e32 v114, v60, v42
	v_add_f32_e32 v115, v61, v43
	s_waitcnt lgkmcnt(2)
	v_mfma_f32_16x16x16_bf16 v[58:61], v[120:121], v[128:129], v[62:65]
	ds_read_b64_tr_b16 v[120:121], v132 offset:36864
	v_exp_f32_e32 v112, v112
	v_exp_f32_e32 v113, v113
	v_exp_f32_e32 v114, v114
	s_waitcnt lgkmcnt(2)
	v_mfma_f32_16x16x16_bf16 v[62:65], v[130:131], v[128:129], v[66:69]
	ds_read_b64_tr_b16 v[116:117], v132 offset:36928
	ds_read_b64_tr_b16 v[128:129], v132 offset:36936
	v_exp_f32_e32 v115, v115
	v_add_f32_e32 v118, v112, v122
	v_add_f32_e32 v119, v113, v123
	v_add_u32_e32 v122, v144, v105
	s_waitcnt lgkmcnt(2)
; #define LAS __attribute__((address_space(3)))
; __device__ __forceinline__ unsigned cvt_pk_bf16(float lo, float hi) { const f32x2_t v = {lo, hi}; return __builtin_bit_cast(unsigned, __builtin_convertvector(v, bf16x2_t)); }
; __device__ __forceinline__ s16x4 tr_read(LAS unsigned char* p) { return __builtin_bit_cast(s16x4, __builtin_amdgcn_ds_read_tr16_b64_v4i16((LAS s16x4*)p)); }
; __device__ __forceinline__ void phase_attn(Frame& F) {
;     ...
;         for (int T = 0; T < 9; ++T) {
;             u32x2 pw; pw.x = cvt_pk_bf16(St[T][0], St[T][1]); pw.y = cvt_pk_bf16(St[T][2], St[T][3]);
;             const s16x4 pb = __builtin_bit_cast(s16x4, pw);
;             LAS unsigned char* va = kb + ATT_VOFF + (16 * (w + T) + 4 * fq + (fr >> 2)) * ATT_ROWB + (8 * (fr & 3)) * 2;
; #pragma unroll
;             for (int dt = 0; dt < 4; ++dt) O[dt] = __builtin_amdgcn_mfma_f32_16x16x16bf16_1k(tr_read(va + 64 * (dt >> 1) + 8 * (dt & 1)), pb, O[dt], 0, 0, 0);
;         }
;         const float inv = 1.f / l;
;         bf16_t* op = (bf16_t*)((char*)part + (((size_t)cu.dsel * NTOK + (size_t)cu.b * SEQ + cu.r) * 512 + cu.h * 64) * 2 + (qrow * 1024u + 16u * fq));
; #pragma unroll
;         for (int u2 = 0; u2 < 2; ++u2) { u32x4 o4; o4.x = cvt_pk_bf16(O[2 * u2][0] * inv, O[2 * u2][1] * inv); o4.y = cvt_pk_bf16(O[2 * u2][2] * inv, O[2 * u2][3] * inv);
;             o4.z = cvt_pk_bf16(O[2 * u2 + 1][0] * inv, O[2 * u2 + 1][1] * inv); o4.w = cvt_pk_bf16(O[2 * u2 + 1][2] * inv, O[2 * u2 + 1][3] * inv); *(u32x4*)(op + 32 * u2) = o4; }
;         if (fq == 0) *(float*)((char*)lse + (((size_t)cu.dsel * NTOK + (size_t)cu.b * SEQ + cu.r) * 8 + cu.h) * 4 + qrow * 32u) = mx + __builtin_amdgcn_logf(l);
;         cu = nu; buf ^= 1;
	v_mfma_f32_16x16x16_bf16 v[66:69], v[120:121], v[126:127], v[70:73]
	ds_read_b64_tr_b16 v[120:121], v122 offset:36872
	v_mfma_f32_16x16x16_bf16 v[70:73], v[124:125], v[126:127], v[74:77]
	s_nop 2
	v_add_f32_e64 v74, v114, v78
	v_add_f32_e64 v75, v115, v79
	v_add_f32_e32 v76, v54, v44
	v_add_f32_e32 v77, v55, v45
	v_add_f32_e32 v78, v56, v42
	v_add_f32_e32 v79, v57, v43
	s_waitcnt lgkmcnt(2)
	v_mfma_f32_16x16x16_bf16 v[54:57], v[116:117], v[126:127], v[58:61]
	ds_read_b64_tr_b16 v[116:117], v122 offset:36864
	v_cvt_pk_bf16_f32 v114, v114, v115
	v_cvt_pk_bf16_f32 v115, v112, v113
	ds_read_b64_tr_b16 v[112:113], v122 offset:36928
	ds_read_b64_tr_b16 v[122:123], v122 offset:36936
	s_waitcnt lgkmcnt(4)
	v_mfma_f32_16x16x16_bf16 v[58:61], v[128:129], v[126:127], v[62:65]
	v_exp_f32_e32 v76, v76
	v_exp_f32_e32 v77, v77
	v_exp_f32_e32 v78, v78
	s_waitcnt lgkmcnt(2)
	v_mfma_f32_16x16x16_bf16 v[62:65], v[116:117], v[114:115], v[66:69]
	v_exp_f32_e32 v79, v79
	v_add_f32_e32 v116, v76, v118
	v_add_f32_e32 v117, v77, v119
	v_mfma_f32_16x16x16_bf16 v[66:69], v[120:121], v[114:115], v[70:73]
	s_nop 2
	v_add_f32_e64 v70, v42, v46
	v_add_f32_e64 v71, v43, v47
	s_waitcnt lgkmcnt(1)
	v_mfma_f32_16x16x16_bf16 v[42:45], v[112:113], v[114:115], v[54:57]
	v_exp_f32_e32 v72, v48
	v_exp_f32_e32 v73, v49
	v_exp_f32_e32 v70, v70
	v_add_u32_e32 v56, v144, v106
	ds_read_b64_tr_b16 v[54:55], v56 offset:36864
	s_waitcnt lgkmcnt(1)
	v_mfma_f32_16x16x16_bf16 v[46:49], v[122:123], v[114:115], v[58:61]
	v_exp_f32_e32 v71, v71
	v_cvt_pk_bf16_f32 v112, v78, v79
	v_cvt_pk_bf16_f32 v113, v76, v77
	ds_read_b64_tr_b16 v[58:59], v56 offset:36872
	ds_read_b64_tr_b16 v[76:77], v56 offset:36928
	ds_read_b64_tr_b16 v[114:115], v56 offset:36936
	s_waitcnt lgkmcnt(3)
	v_mfma_f32_16x16x16_bf16 v[54:57], v[54:55], v[112:113], v[62:65]
	s_nop 2
	v_add_f32_e64 v62, v78, v74
	v_add_f32_e64 v63, v79, v75
	v_add_f32_e32 v64, v72, v116
	v_add_f32_e32 v65, v73, v117
	v_add_f32_e32 v62, v70, v62
	v_add_f32_e32 v63, v71, v63
	v_add_u32_e32 v74, v144, v107
	s_waitcnt lgkmcnt(2)
	v_mfma_f32_16x16x16_bf16 v[58:61], v[58:59], v[112:113], v[66:69]
	s_nop 2
	v_pk_mov_b32 v[66:67], v[62:63], v[64:65] op_sel:[1,0]
	v_mov_b32_e32 v63, v65
	ds_read_b64_tr_b16 v[64:65], v74 offset:36864
	v_add_f32_e32 v62, v66, v62
	v_add_f32_e32 v63, v67, v63
	v_cvt_pk_bf16_f32 v66, v70, v71
	v_add_f32_e32 v75, v62, v63
	v_cvt_pk_bf16_f32 v67, v72, v73
	s_waitcnt lgkmcnt(2)
	v_mfma_f32_16x16x16_bf16 v[42:45], v[76:77], v[112:113], v[42:45]
	ds_read_b64_tr_b16 v[62:63], v74 offset:36872
	ds_read_b64_tr_b16 v[68:69], v74 offset:36928
	ds_read_b64_tr_b16 v[70:71], v74 offset:36936
	s_waitcnt lgkmcnt(3)
	v_mfma_f32_16x16x16_bf16 v[54:57], v[64:65], v[66:67], v[54:57]
	v_mov_b32_e32 v168, v75
	s_waitcnt lgkmcnt(0)
	s_nop 0
	v_permlane16_swap_b32_e32 v168, v75
	v_add_f32_e32 v72, v75, v168
	v_mov_b32_e32 v169, v72
	v_mfma_f32_16x16x16_bf16 v[58:61], v[62:63], v[66:67], v[58:61]
	v_mfma_f32_16x16x16_bf16 v[62:65], v[68:69], v[66:67], v[42:45]
	v_permlane32_swap_b32_e32 v169, v72
	s_nop 1
	v_add_f32_e32 v43, v72, v169
	v_div_scale_f32 v68, s[64:65], v43, v43, 1.0
	v_mfma_f32_16x16x16_bf16 v[46:49], v[114:115], v[112:113], v[46:49]
	v_rcp_f32_e32 v69, v68
	v_lshlrev_b32_e32 v42, s35, v110
	s_ashr_i32 s35, s34, 31
	v_mfma_f32_16x16x16_bf16 v[44:47], v[70:71], v[66:67], v[46:49]
	s_lshl_b64 s[64:65], s[26:27], 16
	s_lshl_b64 s[34:35], s[34:35], 12
	s_ashr_i32 s26, s31, 31
	s_nop 0
	v_fma_f32 v48, -v68, v69, 1.0
	v_fmac_f32_e32 v69, v48, v69
	v_div_scale_f32 v48, vcc, 1.0, v43, 1.0
	v_mul_f32_e32 v49, v48, v69
	s_add_u32 s31, s34, s31
	v_fma_f32 v66, -v68, v49, v48
	s_addc_u32 s26, s35, s26
	v_fmac_f32_e32 v49, v66, v69
	s_add_u32 s34, s31, s64
	v_fma_f32 v48, -v68, v49, v48
	s_addc_u32 s35, s26, s65
	v_div_fmas_f32 v48, v48, v69, v49
	s_lshl_b32 s26, s30, 7
	s_lshl_b64 s[64:65], s[34:35], 10
	v_div_fixup_f32 v48, v48, v43, 1.0
	s_add_u32 s31, s24, s64
	v_lshl_or_b32 v49, v42, 10, v82
	s_addc_u32 s37, s25, s65
	v_mul_f32_e32 v54, v48, v54
	v_mul_f32_e32 v55, v48, v55
	v_mul_f32_e32 v56, v48, v56
	v_mul_f32_e32 v57, v48, v57
	s_add_u32 s64, s31, s26
	v_cvt_pk_bf16_f32 v54, v54, v55
	v_cvt_pk_bf16_f32 v55, v56, v57
	v_mul_f32_e32 v56, v48, v58
	v_mul_f32_e32 v57, v48, v59
	v_mul_f32_e32 v58, v48, v60
	v_mul_f32_e32 v59, v48, v61
	s_addc_u32 s65, s37, 0
	v_cvt_pk_bf16_f32 v56, v56, v57
	v_cvt_pk_bf16_f32 v57, v58, v59
	global_store_dwordx4 v49, v[54:57], s[64:65]
	v_mul_f32_e32 v44, v48, v44
	v_mul_f32_e32 v45, v48, v45
	s_nop 0
	v_mul_f32_e32 v54, v48, v62
	v_mul_f32_e32 v55, v48, v63
	v_mul_f32_e32 v56, v48, v64
	v_mul_f32_e32 v57, v48, v65
	v_cvt_pk_bf16_f32 v54, v54, v55
	v_cvt_pk_bf16_f32 v55, v56, v57
	v_cvt_pk_bf16_f32 v56, v44, v45
	v_mul_f32_e32 v44, v48, v46
	v_mul_f32_e32 v45, v48, v47
	v_cvt_pk_bf16_f32 v57, v44, v45
	global_store_dwordx4 v49, v[54:57], s[64:65] offset:64
	s_and_saveexec_b64 s[64:65], s[4:5]
	s_cbranch_execz .LBB0_303
	s_mov_b32 s31, s27
	v_log_f32_e32 v43, v43
	s_lshl_b64 s[34:35], s[34:35], 5
	s_lshl_b64 s[30:31], s[30:31], 2
	s_add_u32 s26, s67, s34
	s_addc_u32 s34, s68, s35
	s_add_u32 s30, s26, s30
	v_add_f32_e32 v43, v111, v43
	s_addc_u32 s31, s34, s31
	v_lshlrev_b32_e32 v42, 5, v42
	global_store_dword v42, v43, s[30:31]
	s_branch .LBB0_303
